# hot-loop placement: 64-byte alignment of the FFN1, FFN2, attention-a and attention-b main loop heads (padding only)
# speedup vs baseline: 1.0009x; 1.0009x over previous
.Lfastjoin_h2:
	v_fma_f32 v122, v150, s4, 1.0
	v_mov_b32_e32 v123, v122
	v_fmamk_f32 v100, v100, 0x3e0293ee, v122
	v_fmamk_f32 v101, v101, 0x3e0293ee, v122
	v_fmamk_f32 v102, v102, 0x3e0293ee, v122
	v_fmamk_f32 v103, v103, 0x3e0293ee, v122
	v_fmamk_f32 v104, v104, 0x3e0293ee, v122
	v_fmamk_f32 v105, v105, 0x3e0293ee, v122
	v_fmamk_f32 v106, v106, 0x3e0293ee, v122
	v_fmamk_f32 v107, v107, 0x3e0293ee, v122
	v_fmamk_f32 v108, v108, 0x3e0293ee, v122
	v_fmamk_f32 v109, v109, 0x3e0293ee, v122
	v_fmamk_f32 v110, v110, 0x3e0293ee, v122
	v_fmamk_f32 v111, v111, 0x3e0293ee, v122
	v_fmamk_f32 v112, v112, 0x3e0293ee, v122
	v_fmamk_f32 v113, v113, 0x3e0293ee, v122
	v_fmamk_f32 v114, v114, 0x3e0293ee, v122
	v_fmac_f32_e32 v123, 0x3e0293ee, v115
	v_exp_f32_e32 v158, v100
	v_exp_f32_e32 v159, v101
	v_exp_f32_e32 v160, v102
	v_exp_f32_e32 v161, v103
	v_exp_f32_e32 v152, v104
	v_exp_f32_e32 v153, v105
	v_exp_f32_e32 v154, v106
	v_exp_f32_e32 v155, v107
	v_exp_f32_e32 v162, v108
	v_exp_f32_e32 v163, v109
	v_exp_f32_e32 v178, v110
	v_exp_f32_e32 v179, v111
	v_exp_f32_e32 v156, v112
	v_exp_f32_e32 v157, v113
	v_exp_f32_e32 v117, v114
	v_exp_f32_e32 v151, v123
	s_add_u32 s36, s36, 0x8000
	v_pk_fma_f32 v[148:149], v[84:85], s[30:31], v[122:123] op_sel_hi:[1,0,0]
	v_pk_fma_f32 v[142:143], v[86:87], s[30:31], v[122:123] op_sel_hi:[1,0,0]
	v_pk_fma_f32 v[140:141], v[88:89], s[30:31], v[122:123] op_sel_hi:[1,0,0]
	v_pk_fma_f32 v[120:121], v[90:91], s[30:31], v[122:123] op_sel_hi:[1,0,0]
	v_pk_fma_f32 v[118:119], v[92:93], s[30:31], v[122:123] op_sel_hi:[1,0,0]
	v_pk_fma_f32 v[146:147], v[94:95], s[30:31], v[122:123] op_sel_hi:[1,0,0]
	v_pk_fma_f32 v[144:145], v[96:97], s[30:31], v[122:123] op_sel_hi:[1,0,0]
	v_pk_fma_f32 v[122:123], v[98:99], s[30:31], v[122:123] op_sel_hi:[1,0,0]
	s_addc_u32 s37, s37, 0
	s_and_b64 vcc, exec, s[42:43]
	s_waitcnt lgkmcnt(0)
	s_barrier
	s_cbranch_vccnz .LBB0_1297
	.p2align 6

.LBB0_1915:
	v_lshl_add_u64 v[4:5], s[36:37], 0, v[172:173]
	global_load_dword v206, v[4:5], off
	s_add_u32 s0, s36, 0x200
	v_lshl_add_u64 v[4:5], s[36:37], 0, v[174:175]
	global_load_dword v207, v[4:5], off
	s_addc_u32 s1, s37, 0
	v_lshl_add_u64 v[4:5], s[0:1], 0, v[172:173]
	global_load_dword v208, v[4:5], off
	s_add_u32 s6, s50, 0x100
	v_lshl_add_u64 v[4:5], s[0:1], 0, v[174:175]
	global_load_dword v209, v[4:5], off
	s_addc_u32 s43, s51, 0
	s_add_u32 s50, s26, 0x80
	v_mov_b32_e32 v179, v3
	v_mov_b32_e32 v177, v3
	s_addc_u32 s51, s27, 0
	s_mov_b32 s45, -2
	s_branch .Lpeelf1_1917
	.p2align 6

.Lpeelf2_hdr:
	s_add_u32 s49, s54, 0x80
	s_addc_u32 s56, s55, 0
	s_cmp_eq_u32 s47, 12
	s_cselect_b32 s59, s51, s56
	s_cselect_b32 s58, s50, s49
	s_cselect_b32 s57, s53, s1
	s_cselect_b32 s56, s52, s0
	s_add_i32 s78, 0, 0x10400
	v_add_u32_e32 v8, s78, v189
	ds_read_b128 v[12:15], v8
	ds_read_b128 v[16:19], v8 offset:1024
	ds_read_b128 v[4:7], v8 offset:2048
	ds_read_b128 v[8:11], v8 offset:3072
	v_lshl_add_u64 v[20:21], s[54:55], 0, v[180:181]
	s_add_i32 m0, s68, 0xc400
	ds_read_b128 v[206:209], v191 offset:1024
	ds_read_b128 v[210:213], v191 offset:2048
	ds_read_b128 v[214:217], v191 offset:3072
	ds_read_b128 v[218:221], v191 offset:4096
	ds_read_b128 v[230:233], v191 offset:5120
	ds_read_b128 v[234:237], v191 offset:6144
	ds_read_b128 v[240:243], v191 offset:7168
	ds_read_b128 v[244:247], v191 offset:8192
	global_load_lds_dwordx4 v[20:21], off
	v_lshl_add_u64 v[20:21], s[54:55], 0, v[178:179]
	s_add_i32 m0, s68, 0xe400
	s_nop 0
	global_load_lds_dwordx4 v[20:21], off
	s_waitcnt lgkmcnt(8)
	s_barrier
	s_waitcnt lgkmcnt(0)
	s_setprio 1
	s_waitcnt lgkmcnt(0)
	v_mfma_scale_f32_16x16x128_f8f6f4 v[162:165], v[12:19], v[206:213], 0, v117, v185 op_sel_hi:[0,0,0]
	v_mfma_scale_f32_16x16x128_f8f6f4 v[158:161], v[4:11], v[206:213], 0, v117, v185 op_sel_hi:[0,0,0]
	v_mfma_scale_f32_16x16x128_f8f6f4 v[154:157], v[12:19], v[214:221], 0, v117, v185 op_sel_hi:[0,0,0]
	v_mfma_scale_f32_16x16x128_f8f6f4 v[146:149], v[4:11], v[214:221], 0, v117, v185 op_sel_hi:[0,0,0]
	v_mfma_scale_f32_16x16x128_f8f6f4 v[138:141], v[12:19], v[230:237], 0, v117, v185 op_sel_hi:[0,0,0]
	v_mfma_scale_f32_16x16x128_f8f6f4 v[130:133], v[4:11], v[230:237], 0, v117, v185 op_sel_hi:[0,0,0]
	v_mfma_scale_f32_16x16x128_f8f6f4 v[122:125], v[12:19], v[240:247], 0, v117, v185 op_sel_hi:[0,0,0]
	v_mfma_scale_f32_16x16x128_f8f6f4 v[112:115], v[4:11], v[240:247], 0, v117, v185 op_sel_hi:[0,0,0]
	s_setprio 0
	s_barrier
	s_add_i32 s49, 0, 0x14400
	s_add_i32 s78, s78, s63
	v_add_u32_e32 v24, s49, v189
	v_lshl_add_u64 v[202:203], s[56:57], 0, v[168:169]
	s_mov_b32 m0, s78
	ds_read_b128 v[28:31], v24
	ds_read_b128 v[32:35], v24 offset:1024
	ds_read_b128 v[20:23], v24 offset:2048
	ds_read_b128 v[24:27], v24 offset:3072
	global_load_lds_dwordx4 v[202:203], off
	v_lshl_add_u64 v[204:205], s[56:57], 0, v[166:167]
	s_add_i32 m0, s78, 0x2000
	s_nop 0
	global_load_lds_dwordx4 v[204:205], off
	s_barrier
	s_waitcnt lgkmcnt(0)
	s_setprio 1
	s_waitcnt lgkmcnt(0)
	v_mfma_scale_f32_16x16x128_f8f6f4 v[150:153], v[28:35], v[206:213], 0, v117, v185 op_sel_hi:[0,0,0]
	v_mfma_scale_f32_16x16x128_f8f6f4 v[142:145], v[20:27], v[206:213], 0, v117, v185 op_sel_hi:[0,0,0]
	v_mfma_scale_f32_16x16x128_f8f6f4 v[134:137], v[28:35], v[214:221], 0, v117, v185 op_sel_hi:[0,0,0]
	v_mfma_scale_f32_16x16x128_f8f6f4 v[126:129], v[20:27], v[214:221], 0, v117, v185 op_sel_hi:[0,0,0]
	v_mfma_scale_f32_16x16x128_f8f6f4 v[118:121], v[28:35], v[230:237], 0, v117, v185 op_sel_hi:[0,0,0]
	v_mfma_scale_f32_16x16x128_f8f6f4 v[108:111], v[20:27], v[230:237], 0, v117, v185 op_sel_hi:[0,0,0]
	v_mfma_scale_f32_16x16x128_f8f6f4 v[104:107], v[28:35], v[240:247], 0, v117, v185 op_sel_hi:[0,0,0]
	v_mfma_scale_f32_16x16x128_f8f6f4 v[100:103], v[20:27], v[240:247], 0, v117, v185 op_sel_hi:[0,0,0]
	s_setprio 0
	s_mov_b32 m0, s3
	v_lshl_add_u64 v[206:207], s[58:59], 0, v[170:171]
	s_barrier
	ds_read_b128 v[210:213], v191 offset:17408
	ds_read_b128 v[214:217], v191 offset:18432
	ds_read_b128 v[218:221], v191 offset:19456
	ds_read_b128 v[222:225], v191 offset:20480
	ds_read_b128 v[230:233], v191 offset:21504
	ds_read_b128 v[234:237], v191 offset:22528
	ds_read_b128 v[240:243], v191 offset:23552
	ds_read_b128 v[244:247], v191 offset:24576
	global_load_lds_dwordx4 v[206:207], off
	v_lshl_add_u64 v[208:209], s[58:59], 0, v[172:173]
	s_mov_b32 m0, s69
	s_nop 0
	global_load_lds_dwordx4 v[208:209], off
	s_barrier
	s_waitcnt lgkmcnt(0)
	s_setprio 1
	s_waitcnt lgkmcnt(0)
	v_mfma_scale_f32_16x16x128_f8f6f4 v[96:99], v[12:19], v[210:217], 0, v117, v185 op_sel_hi:[0,0,0]
	v_mfma_scale_f32_16x16x128_f8f6f4 v[92:95], v[4:11], v[210:217], 0, v117, v185 op_sel_hi:[0,0,0]
	v_mfma_scale_f32_16x16x128_f8f6f4 v[80:83], v[12:19], v[218:225], 0, v117, v185 op_sel_hi:[0,0,0]
	v_mfma_scale_f32_16x16x128_f8f6f4 v[72:75], v[4:11], v[218:225], 0, v117, v185 op_sel_hi:[0,0,0]
	v_mfma_scale_f32_16x16x128_f8f6f4 v[56:59], v[12:19], v[230:237], 0, v117, v185 op_sel_hi:[0,0,0]
	v_mfma_scale_f32_16x16x128_f8f6f4 v[48:51], v[4:11], v[230:237], 0, v117, v185 op_sel_hi:[0,0,0]
	v_mfma_scale_f32_16x16x128_f8f6f4 v[40:43], v[12:19], v[240:247], 0, v117, v185 op_sel_hi:[0,0,0]
	v_mfma_scale_f32_16x16x128_f8f6f4 v[36:39], v[4:11], v[240:247], 0, v117, v185 op_sel_hi:[0,0,0]
	s_setprio 0
	s_barrier
	s_add_u32 s78, s56, 0x40000
	s_addc_u32 s79, s57, 0
	s_add_i32 s49, s49, s63
	v_lshl_add_u64 v[4:5], s[78:79], 0, v[168:169]
	s_mov_b32 m0, s49
	s_nop 0
	global_load_lds_dwordx4 v[4:5], off
	v_lshl_add_u64 v[4:5], s[78:79], 0, v[166:167]
	s_add_i32 m0, s49, 0x2000
	s_nop 0
	global_load_lds_dwordx4 v[4:5], off
	s_waitcnt vmcnt(6)
	s_barrier
	s_setprio 1
	v_mfma_scale_f32_16x16x128_f8f6f4 v[76:79], v[28:35], v[210:217], 0, v117, v185 op_sel_hi:[0,0,0]
	v_mfma_scale_f32_16x16x128_f8f6f4 v[68:71], v[20:27], v[210:217], 0, v117, v185 op_sel_hi:[0,0,0]
	v_mfma_scale_f32_16x16x128_f8f6f4 v[52:55], v[28:35], v[218:225], 0, v117, v185 op_sel_hi:[0,0,0]
	v_mfma_scale_f32_16x16x128_f8f6f4 v[44:47], v[20:27], v[218:225], 0, v117, v185 op_sel_hi:[0,0,0]
	v_mfma_scale_f32_16x16x128_f8f6f4 v[88:91], v[28:35], v[230:237], 0, v117, v185 op_sel_hi:[0,0,0]
	v_mfma_scale_f32_16x16x128_f8f6f4 v[84:87], v[20:27], v[230:237], 0, v117, v185 op_sel_hi:[0,0,0]
	v_mfma_scale_f32_16x16x128_f8f6f4 v[64:67], v[28:35], v[240:247], 0, v117, v185 op_sel_hi:[0,0,0]
	v_mfma_scale_f32_16x16x128_f8f6f4 v[60:63], v[20:27], v[240:247], 0, v117, v185 op_sel_hi:[0,0,0]
	s_setprio 0
	s_add_i32 s49, 0, 0x18400
	v_add_u32_e32 v8, s49, v189
	s_barrier
	ds_read_b128 v[12:15], v8
	ds_read_b128 v[16:19], v8 offset:1024
	ds_read_b128 v[4:7], v8 offset:2048
	ds_read_b128 v[8:11], v8 offset:3072
	s_mov_b32 m0, s70
	v_lshl_add_u64 v[182:183], s[58:59], 0, v[174:175]
	ds_read_b128 v[20:23], v191 offset:33792
	ds_read_b128 v[24:27], v191 offset:34816
	ds_read_b128 v[28:31], v191 offset:35840
	ds_read_b128 v[32:35], v191 offset:36864
	ds_read_b128 v[210:213], v191 offset:37888
	ds_read_b128 v[214:217], v191 offset:38912
	ds_read_b128 v[218:221], v191 offset:39936
	ds_read_b128 v[222:225], v191 offset:40960
	global_load_lds_dwordx4 v[182:183], off
	v_lshl_add_u64 v[182:183], s[58:59], 0, v[176:177]
	s_mov_b32 m0, s71
	s_nop 0
	global_load_lds_dwordx4 v[182:183], off
	s_waitcnt lgkmcnt(8)
	s_barrier
	s_waitcnt lgkmcnt(0)
	s_setprio 1
	s_waitcnt lgkmcnt(0)
	v_mfma_scale_f32_16x16x128_f8f6f4 v[162:165], v[12:19], v[20:27], v[162:165], v117, v185 op_sel_hi:[0,0,0]
	v_mfma_scale_f32_16x16x128_f8f6f4 v[158:161], v[4:11], v[20:27], v[158:161], v117, v185 op_sel_hi:[0,0,0]
	v_mfma_scale_f32_16x16x128_f8f6f4 v[154:157], v[12:19], v[28:35], v[154:157], v117, v185 op_sel_hi:[0,0,0]
	v_mfma_scale_f32_16x16x128_f8f6f4 v[146:149], v[4:11], v[28:35], v[146:149], v117, v185 op_sel_hi:[0,0,0]
	v_mfma_scale_f32_16x16x128_f8f6f4 v[138:141], v[12:19], v[210:217], v[138:141], v117, v185 op_sel_hi:[0,0,0]
	v_mfma_scale_f32_16x16x128_f8f6f4 v[130:133], v[4:11], v[210:217], v[130:133], v117, v185 op_sel_hi:[0,0,0]
	v_mfma_scale_f32_16x16x128_f8f6f4 v[122:125], v[12:19], v[218:225], v[122:125], v117, v185 op_sel_hi:[0,0,0]
	v_mfma_scale_f32_16x16x128_f8f6f4 v[112:115], v[4:11], v[218:225], v[112:115], v117, v185 op_sel_hi:[0,0,0]
	s_setprio 0
	s_barrier
	s_add_i32 s58, 0, 0x1c400
	v_add_u32_e32 v182, s58, v189
	s_add_i32 s49, s49, s63
	ds_read_b128 v[230:233], v182
	ds_read_b128 v[234:237], v182 offset:1024
	ds_read_b128 v[240:243], v182 offset:2048
	ds_read_b128 v[244:247], v182 offset:3072
	v_lshl_add_u64 v[182:183], v[202:203], 0, s[22:23]
	s_mov_b32 m0, s49
	s_nop 0
	global_load_lds_dwordx4 v[182:183], off
	v_lshl_add_u64 v[182:183], v[204:205], 0, s[22:23]
	s_add_i32 m0, s49, 0x2000
	s_nop 0
	global_load_lds_dwordx4 v[182:183], off
	s_barrier
	s_waitcnt lgkmcnt(0)
	s_setprio 1
	s_waitcnt lgkmcnt(0)
	v_mfma_scale_f32_16x16x128_f8f6f4 v[150:153], v[230:237], v[20:27], v[150:153], v117, v185 op_sel_hi:[0,0,0]
	v_mfma_scale_f32_16x16x128_f8f6f4 v[142:145], v[240:247], v[20:27], v[142:145], v117, v185 op_sel_hi:[0,0,0]
	v_mfma_scale_f32_16x16x128_f8f6f4 v[134:137], v[230:237], v[28:35], v[134:137], v117, v185 op_sel_hi:[0,0,0]
	v_mfma_scale_f32_16x16x128_f8f6f4 v[126:129], v[240:247], v[28:35], v[126:129], v117, v185 op_sel_hi:[0,0,0]
	v_mfma_scale_f32_16x16x128_f8f6f4 v[118:121], v[230:237], v[210:217], v[118:121], v117, v185 op_sel_hi:[0,0,0]
	v_mfma_scale_f32_16x16x128_f8f6f4 v[108:111], v[240:247], v[210:217], v[108:111], v117, v185 op_sel_hi:[0,0,0]
	v_mfma_scale_f32_16x16x128_f8f6f4 v[104:107], v[230:237], v[218:225], v[104:107], v117, v185 op_sel_hi:[0,0,0]
	v_mfma_scale_f32_16x16x128_f8f6f4 v[100:103], v[240:247], v[218:225], v[100:103], v117, v185 op_sel_hi:[0,0,0]
	s_setprio 0
	s_mov_b32 m0, s72
	v_lshl_add_u64 v[182:183], v[206:207], 0, s[22:23]
	s_barrier
	ds_read_b128 v[20:23], v191 offset:50176
	ds_read_b128 v[24:27], v191 offset:51200
	ds_read_b128 v[28:31], v191 offset:52224
	ds_read_b128 v[32:35], v191 offset:53248
	ds_read_b128 v[210:213], v191 offset:54272
	ds_read_b128 v[214:217], v191 offset:55296
	ds_read_b128 v[218:221], v191 offset:56320
	ds_read_b128 v[222:225], v191 offset:57344
	global_load_lds_dwordx4 v[182:183], off
	v_lshl_add_u64 v[182:183], v[208:209], 0, s[22:23]
	s_mov_b32 m0, s73
	s_nop 0
	global_load_lds_dwordx4 v[182:183], off
	s_barrier
	s_waitcnt lgkmcnt(0)
	s_setprio 1
	s_waitcnt lgkmcnt(0)
	v_mfma_scale_f32_16x16x128_f8f6f4 v[96:99], v[12:19], v[20:27], v[96:99], v117, v185 op_sel_hi:[0,0,0]
	v_mfma_scale_f32_16x16x128_f8f6f4 v[92:95], v[4:11], v[20:27], v[92:95], v117, v185 op_sel_hi:[0,0,0]
	v_mfma_scale_f32_16x16x128_f8f6f4 v[80:83], v[12:19], v[28:35], v[80:83], v117, v185 op_sel_hi:[0,0,0]
	v_mfma_scale_f32_16x16x128_f8f6f4 v[72:75], v[4:11], v[28:35], v[72:75], v117, v185 op_sel_hi:[0,0,0]
	v_mfma_scale_f32_16x16x128_f8f6f4 v[56:59], v[12:19], v[210:217], v[56:59], v117, v185 op_sel_hi:[0,0,0]
	v_mfma_scale_f32_16x16x128_f8f6f4 v[48:51], v[4:11], v[210:217], v[48:51], v117, v185 op_sel_hi:[0,0,0]
	v_mfma_scale_f32_16x16x128_f8f6f4 v[40:43], v[12:19], v[218:225], v[40:43], v117, v185 op_sel_hi:[0,0,0]
	v_mfma_scale_f32_16x16x128_f8f6f4 v[36:39], v[4:11], v[218:225], v[36:39], v117, v185 op_sel_hi:[0,0,0]
	s_setprio 0
	s_barrier
	s_add_u32 s56, s56, 0x40080
	s_addc_u32 s57, s57, 0
	s_add_i32 s49, s58, s63
	v_lshl_add_u64 v[4:5], s[56:57], 0, v[168:169]
	s_mov_b32 m0, s49
	s_nop 0
	global_load_lds_dwordx4 v[4:5], off
	v_lshl_add_u64 v[4:5], s[56:57], 0, v[166:167]
	s_add_i32 m0, s49, 0x2000
	s_nop 0
	global_load_lds_dwordx4 v[4:5], off
	s_waitcnt vmcnt(6)
	s_barrier
	s_setprio 1
	v_mfma_scale_f32_16x16x128_f8f6f4 v[76:79], v[230:237], v[20:27], v[76:79], v117, v185 op_sel_hi:[0,0,0]
	v_mfma_scale_f32_16x16x128_f8f6f4 v[68:71], v[240:247], v[20:27], v[68:71], v117, v185 op_sel_hi:[0,0,0]
	v_mfma_scale_f32_16x16x128_f8f6f4 v[52:55], v[230:237], v[28:35], v[52:55], v117, v185 op_sel_hi:[0,0,0]
	v_mfma_scale_f32_16x16x128_f8f6f4 v[44:47], v[240:247], v[28:35], v[44:47], v117, v185 op_sel_hi:[0,0,0]
	v_mfma_scale_f32_16x16x128_f8f6f4 v[88:91], v[230:237], v[210:217], v[88:91], v117, v185 op_sel_hi:[0,0,0]
	v_mfma_scale_f32_16x16x128_f8f6f4 v[84:87], v[240:247], v[210:217], v[84:87], v117, v185 op_sel_hi:[0,0,0]
	v_mfma_scale_f32_16x16x128_f8f6f4 v[64:67], v[230:237], v[218:225], v[64:67], v117, v185 op_sel_hi:[0,0,0]
	v_mfma_scale_f32_16x16x128_f8f6f4 v[60:63], v[240:247], v[218:225], v[60:63], v117, v185 op_sel_hi:[0,0,0]
	s_setprio 0
	s_add_i32 s47, s47, 2
	s_add_u32 s0, s0, 0x100
	s_addc_u32 s1, s1, 0
	s_add_u32 s54, s54, 0x100
	s_addc_u32 s55, s55, 0
	s_cmp_gt_u32 s47, 13
	s_barrier
	s_cbranch_scc0 .LBB0_1984
	s_branch .Lpexit_f2
	.p2align 6

.LBB0_2357:
	v_mul_f32_e32 v41, 0x41000000, v41
	v_max_f32_e32 v44, v41, v44
	v_cndmask_b32_e32 v148, v44, v41, vcc
	s_mov_b32 s0, 0xbe38aa3b
	v_fma_f32 v44, v148, s0, 1.0
	v_fmamk_f32 v20, v20, 0x3e38aa3b, v44
	v_fmamk_f32 v21, v21, 0x3e38aa3b, v44
	v_fmamk_f32 v22, v22, 0x3e38aa3b, v44
	v_fmamk_f32 v23, v23, 0x3e38aa3b, v44
	v_fmamk_f32 v24, v24, 0x3e38aa3b, v44
	v_fmamk_f32 v25, v25, 0x3e38aa3b, v44
	v_fmamk_f32 v26, v26, 0x3e38aa3b, v44
	v_fmamk_f32 v27, v27, 0x3e38aa3b, v44
	v_fmamk_f32 v28, v28, 0x3e38aa3b, v44
	v_fmamk_f32 v29, v29, 0x3e38aa3b, v44
	v_fmamk_f32 v30, v30, 0x3e38aa3b, v44
	v_fmamk_f32 v31, v31, 0x3e38aa3b, v44
	v_fmamk_f32 v32, v32, 0x3e38aa3b, v44
	v_fmamk_f32 v33, v33, 0x3e38aa3b, v44
	v_fmamk_f32 v34, v34, 0x3e38aa3b, v44
	v_fmamk_f32 v35, v35, 0x3e38aa3b, v44
	v_pk_fma_f32 v[52:53], v[4:5], s[28:29], v[44:45] op_sel_hi:[1,0,0]
	v_and_b32_e32 v139, 63, v40
	v_and_b32_e32 v4, 0x3fffffc0, v40
	v_lshlrev_b32_e32 v5, 4, v40
	v_exp_f32_e32 v110, v20
	v_exp_f32_e32 v111, v21
	v_exp_f32_e32 v108, v22
	v_exp_f32_e32 v109, v23
	v_exp_f32_e32 v100, v24
	v_exp_f32_e32 v102, v25
	v_exp_f32_e32 v98, v26
	v_exp_f32_e32 v99, v27
	v_exp_f32_e32 v112, v28
	v_exp_f32_e32 v113, v29
	v_exp_f32_e32 v101, v30
	v_exp_f32_e32 v103, v31
	v_exp_f32_e32 v106, v32
	v_exp_f32_e32 v107, v33
	v_exp_f32_e32 v104, v34
	v_exp_f32_e32 v105, v35
	v_pk_fma_f32 v[54:55], v[6:7], s[28:29], v[44:45] op_sel_hi:[1,0,0]
	v_lshl_add_u32 v138, v4, 2, 0
	v_lshlrev_b32_e32 v4, 3, v139
	v_and_b32_e32 v5, 0xc0, v5
	v_lshlrev_b32_e32 v6, 1, v40
	v_and_or_b32 v5, v4, 24, v5
	v_and_b32_e32 v6, 32, v6
	v_and_b32_e32 v4, 0x100, v4
	s_waitcnt vmcnt(3)
	v_or3_b32 v125, v5, v6, v4
	s_add_i32 s0, 0, 0x400
	v_pk_fma_f32 v[94:95], v[18:19], s[28:29], v[44:45] op_sel_hi:[1,0,0]
	v_pk_fma_f32 v[92:93], v[16:17], s[28:29], v[44:45] op_sel_hi:[1,0,0]
	v_pk_fma_f32 v[96:97], v[14:15], s[28:29], v[44:45] op_sel_hi:[1,0,0]
	v_pk_fma_f32 v[60:61], v[12:13], s[28:29], v[44:45] op_sel_hi:[1,0,0]
	v_pk_fma_f32 v[58:59], v[10:11], s[28:29], v[44:45] op_sel_hi:[1,0,0]
	v_pk_fma_f32 v[56:57], v[8:9], s[28:29], v[44:45] op_sel_hi:[1,0,0]
	v_add_u32_e32 v145, s0, v125
	s_waitcnt vmcnt(1)
	v_perm_b32 v4, v43, v42, s14
	v_perm_b32 v5, v43, v42, s15
	s_andn2_b64 vcc, exec, s[38:39]
	v_cmp_gt_u32_e64 s[38:39], 32, v139
	v_lshl_add_u32 v140, v136, 2, v138
	ds_write_b64 v143, v[4:5] offset:9216
	s_waitcnt vmcnt(0)
	ds_write_b64 v144, v[38:39] offset:25600
	s_waitcnt lgkmcnt(0)
	s_barrier
	s_cbranch_vccnz .LBB0_2379
	v_add_u32_e32 v4, s3, v136
	v_sub_u32_e32 v4, v4, v124
	v_sub_u32_e32 v4, v4, v126
	v_lshl_add_u64 v[132:133], s[70:71], 0, v[36:37]
	s_add_i32 s0, 0, 0x2400
	v_subrev_u32_e32 v147, s8, v4
	v_mov_b32_e32 v36, 2.0
	v_mov_b32_e32 v4, 0
	v_lshl_add_u64 v[130:131], s[72:73], 0, v[2:3]
	v_lshl_add_u32 v2, v124, 2, v138
	v_add_u32_e32 v146, s0, v125
	s_movk_i32 s3, 0x100
	s_mov_b32 s25, -1
	v_mov_b32_e32 v5, v4
	v_mov_b32_e32 v6, v4
	v_mov_b32_e32 v7, v4
	v_mov_b32_e32 v8, v4
	v_mov_b32_e32 v9, v4
	v_mov_b32_e32 v10, v4
	v_mov_b32_e32 v11, v4
	v_mov_b32_e32 v12, v4
	v_mov_b32_e32 v13, v4
	v_mov_b32_e32 v14, v4
	v_mov_b32_e32 v15, v4
	v_mov_b32_e32 v16, v4
	v_mov_b32_e32 v17, v4
	v_mov_b32_e32 v18, v4
	v_mov_b32_e32 v19, v4
	v_mov_b32_e32 v20, v4
	v_mov_b32_e32 v21, v4
	v_mov_b32_e32 v22, v4
	v_mov_b32_e32 v23, v4
	v_mov_b32_e32 v24, v4
	v_mov_b32_e32 v25, v4
	v_mov_b32_e32 v26, v4
	v_mov_b32_e32 v27, v4
	v_mov_b32_e32 v28, v4
	v_mov_b32_e32 v29, v4
	v_mov_b32_e32 v30, v4
	v_mov_b32_e32 v31, v4
	v_mov_b32_e32 v32, v4
	v_mov_b32_e32 v33, v4
	v_mov_b32_e32 v34, v4
	v_mov_b32_e32 v35, v4
	v_mov_b32_e32 v37, v36
	v_mov_b32_e32 v38, v36
	v_mov_b32_e32 v39, v36
	v_mov_b32_e32 v40, v36
	v_mov_b32_e32 v41, v36
	v_mov_b32_e32 v42, v36
	v_mov_b32_e32 v43, v36
	v_mov_b32_e32 v44, v36
	v_mov_b32_e32 v45, v36
	v_mov_b32_e32 v46, v36
	v_mov_b32_e32 v47, v36
	v_mov_b32_e32 v48, v36
	v_mov_b32_e32 v49, v36
	v_mov_b32_e32 v50, v36
	v_mov_b32_e32 v51, v36
	v_mov_b32_e32 v240, v116
	v_mov_b32_e32 v241, v116
	v_mov_b32_e32 v242, v116
	v_mov_b32_e32 v243, v116
	v_mov_b32_e32 v244, v116
	v_mov_b32_e32 v245, v116
	v_mov_b32_e32 v246, v116
	v_mov_b32_e32 v247, v116
	.p2align 6
